# v048 + per-unit accumulator re-zeroing done by the matrix pipe (7 x v_mfma 32x32x16 with zero operands) instead of 127 v_mov, all eight GEMM phases
# baseline (speedup 1.0000x reference)
.LBB0_196:
	s_ashr_i32 s15, s14, 31
	s_lshl_b64 s[16:17], s[14:15], 18
	s_add_u32 s16, s96, s16
	s_addc_u32 s17, s97, s17
	s_and_b64 s[18:19], s[2:3], exec
	s_cselect_b32 s15, s17, s23
	s_cselect_b32 s55, s16, s22
	s_ashr_i32 s13, s12, 31
	s_lshl_b64 s[18:19], s[12:13], 18
	s_add_u32 s18, s6, s18
	s_addc_u32 s19, s7, s19
	s_and_b64 s[26:27], s[2:3], exec
	s_cselect_b32 s13, s19, s25
	s_cselect_b32 s56, s18, s24
	s_add_u32 s22, s22, 0x80
	s_addc_u32 s23, s23, 0
	s_add_u32 s57, s24, 0x100
	v_mov_b32_e32 v2, 0
	s_addc_u32 s63, s25, 0
	s_mov_b32 s64, -2
	s_waitcnt vmcnt(0)
	v_mov_b32_e32 v114, 0
	v_mov_b32_e32 v115, 0
	v_mov_b32_e32 v116, 0
	v_mov_b32_e32 v117, 0
	v_mov_b32_e32 v118, 0
	v_mov_b32_e32 v119, 0
	v_mov_b32_e32 v120, 0
	v_mov_b32_e32 v121, 0
	v_mov_b32_e32 v122, 0
	v_mov_b32_e32 v123, 0
	v_mov_b32_e32 v124, 0
	v_mov_b32_e32 v125, 0
	v_mov_b32_e32 v126, 0
	v_mov_b32_e32 v127, 0
	v_mov_b32_e32 v128, 0
	v_mov_b32_e32 v129, 0
	s_nop 1
	v_mfma_f32_32x32x16_bf16 v[2:17], v[114:117], v[114:117], 0
	v_mfma_f32_32x32x16_bf16 v[18:33], v[114:117], v[114:117], 0
	v_mfma_f32_32x32x16_bf16 v[34:49], v[114:117], v[114:117], 0
	v_mfma_f32_32x32x16_bf16 v[50:65], v[114:117], v[114:117], 0
	v_mfma_f32_32x32x16_bf16 v[66:81], v[114:117], v[114:117], 0
	v_mfma_f32_32x32x16_bf16 v[82:97], v[114:117], v[114:117], 0
	v_mfma_f32_32x32x16_bf16 v[98:113], v[114:117], v[114:117], 0

.LBB0_348:
	s_ashr_i32 s11, s10, 31
	s_lshl_b64 s[12:13], s[10:11], 19
	s_add_u32 s12, s92, s12
	s_addc_u32 s13, s93, s13
	s_and_b64 s[14:15], s[2:3], exec
	s_cselect_b32 s11, s13, s21
	s_cselect_b32 s49, s12, s20
	s_ashr_i32 s9, s8, 31
	s_lshl_b64 s[14:15], s[8:9], 19
	s_add_u32 s14, s40, s14
	s_addc_u32 s15, s41, s15
	s_and_b64 s[22:23], s[2:3], exec
	s_cselect_b32 s9, s15, s19
	s_cselect_b32 s50, s14, s18
	s_add_u32 s20, s20, 0x80
	s_addc_u32 s21, s21, 0
	s_add_u32 s51, s18, 0x100
	v_mov_b32_e32 v66, 0
	s_addc_u32 s52, s19, 0
	s_mov_b32 s53, -2
	s_waitcnt vmcnt(0)
	v_mov_b32_e32 v114, 0
	v_mov_b32_e32 v115, 0
	v_mov_b32_e32 v116, 0
	v_mov_b32_e32 v117, 0
	v_mov_b32_e32 v118, 0
	v_mov_b32_e32 v119, 0
	v_mov_b32_e32 v120, 0
	v_mov_b32_e32 v121, 0
	v_mov_b32_e32 v130, 0
	v_mov_b32_e32 v131, 0
	v_mov_b32_e32 v132, 0
	v_mov_b32_e32 v133, 0
	v_mov_b32_e32 v134, 0
	v_mov_b32_e32 v135, 0
	v_mov_b32_e32 v136, 0
	v_mov_b32_e32 v137, 0
	s_nop 1
	v_mfma_f32_32x32x16_bf16 v[2:17], v[114:117], v[114:117], 0
	v_mfma_f32_32x32x16_bf16 v[18:33], v[114:117], v[114:117], 0
	v_mfma_f32_32x32x16_bf16 v[34:49], v[114:117], v[114:117], 0
	v_mfma_f32_32x32x16_bf16 v[50:65], v[114:117], v[114:117], 0
	v_mfma_f32_32x32x16_bf16 v[66:81], v[114:117], v[114:117], 0
	v_mfma_f32_32x32x16_bf16 v[82:97], v[114:117], v[114:117], 0
	v_mfma_f32_32x32x16_bf16 v[98:113], v[114:117], v[114:117], 0

.LBB0_504:
	s_lshl_b64 s[24:25], s[0:1], 21
	s_add_u32 s1, s61, s24
	s_addc_u32 s29, s62, s25
	s_ashr_i32 s21, s20, 31
	s_lshl_b64 s[24:25], s[20:21], 18
	s_add_u32 s24, s1, s24
	s_addc_u32 s25, s29, s25
	s_and_b64 s[30:31], s[22:23], exec
	s_cselect_b32 s1, s25, s19
	s_cselect_b32 s21, s24, s18
	s_add_u32 s29, s18, 0x100
	v_mov_b32_e32 v42, v188
	v_mov_b32_e32 v43, v167
	v_mov_b32_e32 v44, v187
	v_mov_b32_e32 v45, v167
	s_addc_u32 s57, s19, 0
	s_mov_b32 s63, -2
	s_mov_b64 s[40:41], s[8:9]
	s_waitcnt vmcnt(0)
	v_mov_b32_e32 v187, v3
	v_mov_b32_e32 v188, v2
	v_mov_b32_e32 v34, 0
	v_mov_b32_e32 v35, 0
	v_mov_b32_e32 v36, 0
	v_mov_b32_e32 v37, 0
	v_mov_b32_e32 v38, 0
	v_mov_b32_e32 v39, 0
	v_mov_b32_e32 v40, 0
	v_mov_b32_e32 v41, 0
	v_mov_b32_e32 v58, 0
	v_mov_b32_e32 v59, 0
	v_mov_b32_e32 v60, 0
	v_mov_b32_e32 v61, 0
	v_mov_b32_e32 v62, 0
	v_mov_b32_e32 v63, 0
	v_mov_b32_e32 v64, 0
	v_mov_b32_e32 v65, 0
	s_nop 1
	v_mfma_f32_32x32x16_bf16 v[2:17], v[34:37], v[34:37], 0
	v_mfma_f32_32x32x16_bf16 v[18:33], v[34:37], v[34:37], 0
	v_mfma_f32_32x32x16_bf16 v[82:97], v[34:37], v[34:37], 0
	v_mfma_f32_32x32x16_bf16 v[98:113], v[34:37], v[34:37], 0
	v_mfma_f32_32x32x16_bf16 v[114:129], v[34:37], v[34:37], 0
	v_mfma_f32_32x32x16_bf16 v[130:145], v[34:37], v[34:37], 0
	v_mfma_f32_32x32x16_bf16 v[146:161], v[34:37], v[34:37], 0
	s_branch .LBB0_507

.LBB0_586:
	s_ashr_i32 s11, s10, 31
	s_lshl_b64 s[20:21], s[10:11], 18
	s_add_u32 s20, s94, s20
	s_addc_u32 s21, s95, s21
	s_and_b64 s[24:25], s[14:15], exec
	s_cselect_b32 s11, s21, s23
	s_cselect_b32 s41, s20, s22
	s_ashr_i32 s1, s0, 31
	s_lshl_b64 s[24:25], s[0:1], 20
	s_add_u32 s1, s33, s24
	s_addc_u32 s36, s60, s25
	s_ashr_i32 s13, s12, 31
	s_lshl_b64 s[24:25], s[12:13], 18
	s_add_u32 s24, s1, s24
	s_addc_u32 s25, s36, s25
	s_and_b64 s[36:37], s[14:15], exec
	s_cselect_b32 s1, s25, s19
	s_cselect_b32 s13, s24, s18
	s_add_u32 s22, s22, 0x80
	s_addc_u32 s23, s23, 0
	s_add_u32 s18, s18, 0x100
	v_mov_b32_e32 v98, 0
	s_addc_u32 s19, s19, 0
	s_mov_b32 s57, -2
	v_mov_b32_e32 v146, 0
	v_mov_b32_e32 v147, 0
	v_mov_b32_e32 v148, 0
	v_mov_b32_e32 v149, 0
	v_mov_b32_e32 v150, 0
	v_mov_b32_e32 v151, 0
	v_mov_b32_e32 v152, 0
	v_mov_b32_e32 v153, 0
	v_mov_b32_e32 v154, 0
	v_mov_b32_e32 v155, 0
	v_mov_b32_e32 v156, 0
	v_mov_b32_e32 v157, 0
	v_mov_b32_e32 v158, 0
	v_mov_b32_e32 v159, 0
	v_mov_b32_e32 v160, 0
	v_mov_b32_e32 v161, 0
	s_nop 1
	v_mfma_f32_32x32x16_bf16 v[34:49], v[146:149], v[146:149], 0
	v_mfma_f32_32x32x16_bf16 v[50:65], v[146:149], v[146:149], 0
	v_mfma_f32_32x32x16_bf16 v[66:81], v[146:149], v[146:149], 0
	v_mfma_f32_32x32x16_bf16 v[82:97], v[146:149], v[146:149], 0
	v_mfma_f32_32x32x16_bf16 v[98:113], v[146:149], v[146:149], 0
	v_mfma_f32_32x32x16_bf16 v[114:129], v[146:149], v[146:149], 0
	v_mfma_f32_32x32x16_bf16 v[130:145], v[146:149], v[146:149], 0

.LBB0_729:
	s_ashr_i32 s13, s12, 31
	s_lshl_b64 s[14:15], s[12:13], 18
	s_add_u32 s14, s96, s14
	s_addc_u32 s15, s97, s15
	s_and_b64 s[16:17], s[2:3], exec
	s_cselect_b32 s13, s15, s23
	s_cselect_b32 s46, s14, s22
	s_ashr_i32 s11, s10, 31
	s_lshl_b64 s[16:17], s[10:11], 18
	s_add_u32 s16, s38, s16
	s_addc_u32 s17, s39, s17
	s_and_b64 s[24:25], s[2:3], exec
	s_cselect_b32 s11, s17, s19
	s_cselect_b32 s47, s16, s18
	s_add_u32 s22, s22, 0x80
	s_addc_u32 s23, s23, 0
	s_add_u32 s48, s18, 0x100
	v_mov_b32_e32 v2, 0
	s_addc_u32 s49, s19, 0
	s_mov_b32 s50, -2
	s_waitcnt vmcnt(0)
	v_mov_b32_e32 v50, 0
	v_mov_b32_e32 v51, 0
	v_mov_b32_e32 v52, 0
	v_mov_b32_e32 v53, 0
	v_mov_b32_e32 v54, 0
	v_mov_b32_e32 v55, 0
	v_mov_b32_e32 v56, 0
	v_mov_b32_e32 v57, 0
	v_mov_b32_e32 v58, 0
	v_mov_b32_e32 v59, 0
	v_mov_b32_e32 v60, 0
	v_mov_b32_e32 v61, 0
	v_mov_b32_e32 v70, 0
	v_mov_b32_e32 v71, 0
	v_mov_b32_e32 v72, 0
	v_mov_b32_e32 v73, 0
	s_nop 1
	v_mfma_f32_32x32x16_bf16 v[2:17], v[50:53], v[50:53], 0
	v_mfma_f32_32x32x16_bf16 v[18:33], v[50:53], v[50:53], 0
	v_mfma_f32_32x32x16_bf16 v[34:49], v[50:53], v[50:53], 0
	v_mfma_f32_32x32x16_bf16 v[82:97], v[50:53], v[50:53], 0
	v_mfma_f32_32x32x16_bf16 v[98:113], v[50:53], v[50:53], 0
	v_mfma_f32_32x32x16_bf16 v[114:129], v[50:53], v[50:53], 0
	v_mfma_f32_32x32x16_bf16 v[130:145], v[50:53], v[50:53], 0

.LBB0_2920:
	s_ashr_i32 s11, s10, 31
	s_lshl_b64 s[12:13], s[10:11], 19
	s_add_u32 s12, s92, s12
	s_addc_u32 s13, s93, s13
	s_and_b64 s[14:15], s[2:3], exec
	s_cselect_b32 s11, s13, s21
	s_cselect_b32 s44, s12, s20
	s_ashr_i32 s9, s8, 31
	s_lshl_b64 s[14:15], s[8:9], 19
	v_readlane_b32 s22, v252, 51
	v_readlane_b32 s23, v252, 52
	s_add_u32 s14, s22, s14
	s_addc_u32 s15, s23, s15
	s_and_b64 s[22:23], s[2:3], exec
	s_cselect_b32 s9, s15, s19
	s_cselect_b32 s45, s14, s18
	s_add_u32 s20, s20, 0x80
	s_addc_u32 s21, s21, 0
	s_add_u32 s46, s18, 0x100
	s_waitcnt vmcnt(0)
	v_mov_b32_e32 v30, 0
	s_addc_u32 s47, s19, 0
	s_mov_b32 s48, -2
	s_waitcnt lgkmcnt(0)
	v_mov_b32_e32 v114, 0
	v_mov_b32_e32 v115, 0
	v_mov_b32_e32 v116, 0
	v_mov_b32_e32 v117, 0
	v_mov_b32_e32 v118, 0
	v_mov_b32_e32 v119, 0
	v_mov_b32_e32 v120, 0
	v_mov_b32_e32 v121, 0
	v_mov_b32_e32 v122, 0
	v_mov_b32_e32 v123, 0
	v_mov_b32_e32 v124, 0
	v_mov_b32_e32 v125, 0
	v_mov_b32_e32 v126, 0
	v_mov_b32_e32 v127, 0
	v_mov_b32_e32 v128, 0
	v_mov_b32_e32 v129, 0
	s_nop 1
	v_mfma_f32_32x32x16_bf16 v[2:17], v[114:117], v[114:117], 0
	v_mfma_f32_32x32x16_bf16 v[18:33], v[114:117], v[114:117], 0
	v_mfma_f32_32x32x16_bf16 v[34:49], v[114:117], v[114:117], 0
	v_mfma_f32_32x32x16_bf16 v[50:65], v[114:117], v[114:117], 0
	v_mfma_f32_32x32x16_bf16 v[66:81], v[114:117], v[114:117], 0
	v_mfma_f32_32x32x16_bf16 v[82:97], v[114:117], v[114:117], 0
	v_mfma_f32_32x32x16_bf16 v[98:113], v[114:117], v[114:117], 0

.LBB0_3076:
	s_lshl_b64 s[20:21], s[0:1], 21
	s_add_u32 s1, s33, s20
	s_addc_u32 s27, s36, s21
	s_ashr_i32 s19, s18, 31
	s_lshl_b64 s[20:21], s[18:19], 18
	s_add_u32 s20, s1, s20
	s_addc_u32 s21, s27, s21
	s_and_b64 s[30:31], s[22:23], exec
	s_cselect_b32 s1, s21, s29
	s_cselect_b32 s19, s20, s28
	s_add_u32 s27, s28, 0x100
	v_mov_b32_e32 v74, v177
	v_mov_b32_e32 v75, v167
	v_mov_b32_e32 v76, v176
	v_mov_b32_e32 v77, v167
	s_addc_u32 s58, s29, 0
	s_mov_b32 s59, -2
	s_mov_b64 s[28:29], s[8:9]
	s_waitcnt vmcnt(0)
	v_mov_b32_e32 v176, v3
	v_mov_b32_e32 v177, v2
	v_mov_b32_e32 v66, 0
	v_mov_b32_e32 v67, 0
	v_mov_b32_e32 v68, 0
	v_mov_b32_e32 v69, 0
	v_mov_b32_e32 v70, 0
	v_mov_b32_e32 v71, 0
	v_mov_b32_e32 v72, 0
	v_mov_b32_e32 v73, 0
	v_mov_b32_e32 v78, 0
	v_mov_b32_e32 v79, 0
	v_mov_b32_e32 v80, 0
	v_mov_b32_e32 v81, 0
	v_mov_b32_e32 v94, 0
	v_mov_b32_e32 v95, 0
	v_mov_b32_e32 v96, 0
	v_mov_b32_e32 v97, 0
	v_mov_b32_e32 v102, 0
	v_mov_b32_e32 v103, 0
	v_mov_b32_e32 v104, 0
	v_mov_b32_e32 v105, 0
	v_mov_b32_e32 v150, 0
	v_mov_b32_e32 v151, 0
	v_mov_b32_e32 v152, 0
	v_mov_b32_e32 v153, 0
	v_mov_b32_e32 v154, 0
	v_mov_b32_e32 v155, 0
	v_mov_b32_e32 v156, 0
	v_mov_b32_e32 v157, 0
	v_mov_b32_e32 v158, 0
	v_mov_b32_e32 v159, 0
	v_mov_b32_e32 v160, 0
	v_mov_b32_e32 v161, 0
	s_nop 1
	v_mfma_f32_32x32x16_bf16 v[2:17], v[66:69], v[66:69], 0
	v_mfma_f32_32x32x16_bf16 v[18:33], v[66:69], v[66:69], 0
	v_mfma_f32_32x32x16_bf16 v[34:49], v[66:69], v[66:69], 0
	v_mfma_f32_32x32x16_bf16 v[50:65], v[66:69], v[66:69], 0
	v_mfma_f32_32x32x16_bf16 v[118:133], v[66:69], v[66:69], 0
	v_mfma_f32_32x32x16_bf16 v[134:149], v[66:69], v[66:69], 0
	s_branch .LBB0_3079

.LBB0_3158:
	s_ashr_i32 s11, s10, 31
	s_lshl_b64 s[18:19], s[10:11], 18
	s_add_u32 s18, s94, s18
	s_addc_u32 s19, s95, s19
	s_and_b64 s[20:21], s[14:15], exec
	s_cselect_b32 s11, s19, s29
	s_cselect_b32 s27, s18, s28
	s_ashr_i32 s1, s0, 31
	s_lshl_b64 s[20:21], s[0:1], 20
	s_add_u32 s1, s34, s20
	s_addc_u32 s36, s35, s21
	s_ashr_i32 s13, s12, 31
	s_lshl_b64 s[20:21], s[12:13], 18
	s_add_u32 s20, s1, s20
	s_addc_u32 s21, s36, s21
	s_and_b64 s[36:37], s[14:15], exec
	s_cselect_b32 s1, s21, s31
	s_cselect_b32 s13, s20, s30
	s_add_u32 s28, s28, 0x80
	s_addc_u32 s29, s29, 0
	s_add_u32 s30, s30, 0x100
	v_mov_b32_e32 v94, 0
	s_addc_u32 s31, s31, 0
	s_mov_b32 s58, -2
	v_mov_b32_e32 v146, 0
	v_mov_b32_e32 v147, 0
	v_mov_b32_e32 v148, 0
	v_mov_b32_e32 v149, 0
	v_mov_b32_e32 v150, 0
	v_mov_b32_e32 v151, 0
	v_mov_b32_e32 v152, 0
	v_mov_b32_e32 v153, 0
	v_mov_b32_e32 v154, 0
	v_mov_b32_e32 v155, 0
	v_mov_b32_e32 v156, 0
	v_mov_b32_e32 v157, 0
	v_mov_b32_e32 v158, 0
	v_mov_b32_e32 v159, 0
	v_mov_b32_e32 v160, 0
	v_mov_b32_e32 v161, 0
	s_nop 1
	v_mfma_f32_32x32x16_bf16 v[34:49], v[146:149], v[146:149], 0
	v_mfma_f32_32x32x16_bf16 v[50:65], v[146:149], v[146:149], 0
	v_mfma_f32_32x32x16_bf16 v[66:81], v[146:149], v[146:149], 0
	v_mfma_f32_32x32x16_bf16 v[82:97], v[146:149], v[146:149], 0
	v_mfma_f32_32x32x16_bf16 v[98:113], v[146:149], v[146:149], 0
	v_mfma_f32_32x32x16_bf16 v[114:129], v[146:149], v[146:149], 0
	v_mfma_f32_32x32x16_bf16 v[130:145], v[146:149], v[146:149], 0
